# E5b squeezed to 72 VGPRs (7 waves per SIMD): transposition addresses in v68/v70/v71, warm-up load lands in v28
# speedup vs baseline: 1.0050x; 1.0050x over previous
.LBB1_6:
	s_or_b64 exec, exec, s[10:11]
	v_lshrrev_b32_e32 v10, 6, v0
	v_lshlrev_b32_e32 v4, 7, v10
	v_lshrrev_b32_e32 v32, 1, v1
	v_lshl_or_b32 v71, s5, 9, v4
	v_mov_b32_e32 v69, 0
	s_waitcnt lgkmcnt(0)
	v_cmp_gt_u32_e32 vcc, 64, v0
	v_lshlrev_b32_e32 v6, 4, v1
	v_mov_b32_e32 v7, v69
	s_and_saveexec_b64 s[10:11], vcc
	s_cbranch_execz .Lwarm_skip
	global_load_dword v28, v[2:3], off
.Lwarm_skip:
	s_or_b64 exec, exec, s[10:11]
	v_mad_u64_u32 v[2:3], s[6:7], v71, 12, s[6:7]
	v_lshlrev_b32_e32 v4, 2, v71
	v_mov_b32_e32 v5, v69
	s_movk_i32 s6, 0xfe00
	v_lshl_add_u64 v[4:5], s[8:9], 0, v[4:5]
	v_lshl_add_u64 v[8:9], v[2:3], 0, v[6:7]
	s_mov_b32 s7, -1
	v_lshl_add_u64 v[4:5], v[4:5], 0, v[6:7]
	v_lshl_add_u64 v[2:3], v[8:9], 0, s[6:7]
	v_cmp_gt_u32_e32 vcc, 32, v1
	v_lshlrev_b32_e32 v33, 12, v10
	v_add_u32_e32 v34, v33, v6
	v_cndmask_b32_e32 v3, v3, v5, vcc
	v_cndmask_b32_e32 v2, v2, v4, vcc
	global_load_dwordx4 v[2:5], v[2:3], off
	v_and_b32_e32 v44, 1, v0
	v_lshl_add_u32 v0, v32, 4, v33
	v_lshlrev_b32_e32 v68, 4, v32
	v_lshlrev_b32_e32 v12, 6, v44
	v_xor_b32_e32 v68, v68, v12
	v_lshl_add_u32 v68, v44, 11, v68
	v_lshl_add_u32 v68, v10, 12, v68
	v_and_b32_e32 v12, 31, v1
	v_lshrrev_b32_e32 v13, 5, v1
	v_lshl_or_b32 v14, v12, 2, v71
	v_lshlrev_b32_e32 v15, 7, v71
	v_and_b32_e32 v15, 0xe000000, v15
	v_and_b32_e32 v14, 0x3fffc, v14
	v_lshlrev_b32_e32 v70, 21, v13
	v_or3_b32 v70, v15, v70, v14
	v_lshlrev_b32_e32 v70, 2, v70
	v_lshlrev_b32_e32 v71, 4, v12
	v_lshlrev_b32_e32 v14, 6, v13
	v_xor_b32_e32 v71, v71, v14
	v_lshl_add_u32 v71, v13, 11, v71
	v_lshl_add_u32 v71, v10, 12, v71
	s_mul_i32 s6, s4, 0x138800
	s_mul_hi_i32 s5, s4, 0x138800
	s_add_u32 s2, s2, s6
	s_addc_u32 s3, s3, s5
	global_load_dwordx4 v[28:31], v[8:9], off offset:512
	s_waitcnt vmcnt(1)
	ds_write_b128 v34, v[2:5]
	ds_read_b128 v[4:7], v0
	v_lshlrev_b32_e32 v0, 4, v44
	s_waitcnt lgkmcnt(0)
	v_max_i32_e32 v1, 0, v4
	v_max_i32_e32 v2, 0, v5
	v_max_i32_e32 v3, 0, v6
	v_max_i32_e32 v8, 0, v7
	v_lshl_or_b32 v35, v1, 7, v0
	v_lshl_or_b32 v36, v2, 7, v0
	v_lshl_or_b32 v37, v3, 7, v0
	v_lshl_or_b32 v38, v8, 7, v0
	global_load_dwordx4 v[20:23], v35, s[2:3]
	global_load_dwordx4 v[16:19], v35, s[2:3] offset:32
	global_load_dwordx4 v[8:11], v35, s[2:3] offset:64
	global_load_dwordx4 v[64:67], v36, s[2:3]
	global_load_dwordx4 v[60:63], v36, s[2:3] offset:32
	global_load_dwordx4 v[56:59], v36, s[2:3] offset:64
	global_load_dwordx4 v[52:55], v37, s[2:3]
	global_load_dwordx4 v[48:51], v37, s[2:3] offset:32
	global_load_dwordx4 v[44:47], v37, s[2:3] offset:64
	global_load_dwordx4 v[24:27], v38, s[2:3]
	global_load_dwordx4 v[12:15], v38, s[2:3] offset:32
	global_load_dwordx4 v[0:3], v38, s[2:3] offset:64
	s_waitcnt vmcnt(12)
	ds_write_b128 v34, v[28:31] offset:1024
	v_mul_u32_u24_e32 v28, 48, v32
	v_cmp_lt_i32_e32 vcc, -1, v4
	v_add_u32_e32 v31, v33, v28
	v_mov_b32_e32 v28, 0
	s_and_saveexec_b64 s[2:3], vcc
	ds_read_b32 v28, v31 offset:512
	s_or_b64 exec, exec, s[2:3]
	s_and_saveexec_b64 s[2:3], vcc
	ds_read_b32 v69, v31 offset:516
	s_or_b64 exec, exec, s[2:3]
	v_mov_b32_e32 v29, 0
	v_mov_b32_e32 v4, 0
	s_and_saveexec_b64 s[2:3], vcc
	ds_read_b32 v4, v31 offset:520
	s_or_b64 exec, exec, s[2:3]
	s_waitcnt vmcnt(11) lgkmcnt(0)
	v_fma_mix_f32 v30, v28, v20, v29 op_sel_hi:[0,1,0]
	v_fma_mix_f32 v20, v28, v20, v29 op_sel:[0,1,0] op_sel_hi:[0,1,0]
	v_fma_mix_f32 v32, v28, v21, v29 op_sel_hi:[0,1,0]
	v_fma_mix_f32 v21, v28, v21, v29 op_sel:[0,1,0] op_sel_hi:[0,1,0]
	v_fma_mix_f32 v33, v28, v22, v29 op_sel_hi:[0,1,0]
	v_fma_mix_f32 v22, v28, v22, v29 op_sel:[0,1,0] op_sel_hi:[0,1,0]
	v_fma_mix_f32 v34, v28, v23, v29 op_sel_hi:[0,1,0]
	v_fma_mix_f32 v23, v28, v23, v29 op_sel:[0,1,0] op_sel_hi:[0,1,0]
	s_waitcnt vmcnt(10)
	v_fma_mix_f32 v28, v69, v16, v30 op_sel_hi:[0,1,0]
	v_fma_mix_f32 v16, v69, v16, v20 op_sel:[0,1,0] op_sel_hi:[0,1,0]
	v_fma_mix_f32 v20, v69, v17, v32 op_sel_hi:[0,1,0]
	v_cmp_lt_i32_e32 vcc, -1, v5
	v_fma_mix_f32 v17, v69, v17, v21 op_sel:[0,1,0] op_sel_hi:[0,1,0]
	v_fma_mix_f32 v21, v69, v18, v33 op_sel_hi:[0,1,0]
	v_fma_mix_f32 v18, v69, v18, v22 op_sel:[0,1,0] op_sel_hi:[0,1,0]
	v_fma_mix_f32 v22, v69, v19, v34 op_sel_hi:[0,1,0]
	v_fma_mix_f32 v19, v69, v19, v23 op_sel:[0,1,0] op_sel_hi:[0,1,0]
	s_waitcnt vmcnt(9)
	v_fma_mix_f32 v40, v4, v8, v28 op_sel_hi:[0,1,0]
	v_fma_mix_f32 v36, v4, v8, v16 op_sel:[0,1,0] op_sel_hi:[0,1,0]
	v_fma_mix_f32 v32, v4, v9, v20 op_sel_hi:[0,1,0]
	v_fma_mix_f32 v28, v4, v9, v17 op_sel:[0,1,0] op_sel_hi:[0,1,0]
	v_fma_mix_f32 v20, v4, v10, v21 op_sel_hi:[0,1,0]
	v_fma_mix_f32 v16, v4, v10, v18 op_sel:[0,1,0] op_sel_hi:[0,1,0]
	v_fma_mix_f32 v8, v4, v11, v22 op_sel_hi:[0,1,0]
	v_fma_mix_f32 v4, v4, v11, v19 op_sel:[0,1,0] op_sel_hi:[0,1,0]
	s_and_saveexec_b64 s[2:3], vcc
	ds_read_b32 v29, v31 offset:524
	s_or_b64 exec, exec, s[2:3]
	v_mov_b32_e32 v5, 0
	v_mov_b32_e32 v9, 0
	s_and_saveexec_b64 s[2:3], vcc
	ds_read_b32 v9, v31 offset:528
	s_or_b64 exec, exec, s[2:3]
	s_and_saveexec_b64 s[2:3], vcc
	ds_read_b32 v5, v31 offset:532
	s_or_b64 exec, exec, s[2:3]
	v_mov_b32_e32 v10, 0
	s_waitcnt vmcnt(8) lgkmcnt(0)
	v_fma_mix_f32 v18, v29, v65, v10 op_sel_hi:[0,1,0]
	v_fma_mix_f32 v17, v29, v64, v10 op_sel:[0,1,0] op_sel_hi:[0,1,0]
	v_fma_mix_f32 v21, v29, v66, v10 op_sel_hi:[0,1,0]
	v_fma_mix_f32 v11, v29, v64, v10 op_sel_hi:[0,1,0]
	v_fma_mix_f32 v19, v29, v65, v10 op_sel:[0,1,0] op_sel_hi:[0,1,0]
	s_waitcnt vmcnt(7)
	v_fma_mix_f32 v18, v9, v61, v18 op_sel_hi:[0,1,0]
	v_fma_mix_f32 v22, v29, v66, v10 op_sel:[0,1,0] op_sel_hi:[0,1,0]
	v_fma_mix_f32 v23, v29, v67, v10 op_sel_hi:[0,1,0]
	v_fma_mix_f32 v29, v29, v67, v10 op_sel:[0,1,0] op_sel_hi:[0,1,0]
	v_fma_mix_f32 v17, v9, v60, v17 op_sel:[0,1,0] op_sel_hi:[0,1,0]
	v_fma_mix_f32 v21, v9, v62, v21 op_sel_hi:[0,1,0]
	s_waitcnt vmcnt(6)
	v_fma_mix_f32 v33, v5, v57, v18 op_sel_hi:[0,1,0]
	v_cmp_lt_i32_e32 vcc, -1, v6
	v_mov_b32_e32 v18, 0
	v_fma_mix_f32 v11, v9, v60, v11 op_sel_hi:[0,1,0]
	v_fma_mix_f32 v19, v9, v61, v19 op_sel:[0,1,0] op_sel_hi:[0,1,0]
	v_fma_mix_f32 v22, v9, v62, v22 op_sel:[0,1,0] op_sel_hi:[0,1,0]
	v_fma_mix_f32 v23, v9, v63, v23 op_sel_hi:[0,1,0]
	v_fma_mix_f32 v30, v9, v63, v29 op_sel:[0,1,0] op_sel_hi:[0,1,0]
	v_fma_mix_f32 v37, v5, v56, v17 op_sel:[0,1,0] op_sel_hi:[0,1,0]
	s_nop 0
	v_fma_mix_f32 v41, v5, v56, v11 op_sel_hi:[0,1,0]
	v_fma_mix_f32 v29, v5, v57, v19 op_sel:[0,1,0] op_sel_hi:[0,1,0]
	v_fma_mix_f32 v21, v5, v58, v21 op_sel_hi:[0,1,0]
	v_fma_mix_f32 v17, v5, v58, v22 op_sel:[0,1,0] op_sel_hi:[0,1,0]
	v_fma_mix_f32 v9, v5, v59, v23 op_sel_hi:[0,1,0]
	v_fma_mix_f32 v5, v5, v59, v30 op_sel:[0,1,0] op_sel_hi:[0,1,0]
	s_and_saveexec_b64 s[2:3], vcc
	ds_read_b32 v18, v31 offset:536
	s_or_b64 exec, exec, s[2:3]
	s_and_saveexec_b64 s[2:3], vcc
	ds_read_b32 v10, v31 offset:540
	s_or_b64 exec, exec, s[2:3]
	v_mov_b32_e32 v11, 0
	v_mov_b32_e32 v6, 0
	s_and_saveexec_b64 s[2:3], vcc
	ds_read_b32 v6, v31 offset:544
	s_or_b64 exec, exec, s[2:3]
	s_waitcnt vmcnt(5) lgkmcnt(0)
	v_fma_mix_f32 v22, v18, v52, v11 op_sel:[0,1,0] op_sel_hi:[0,1,0]
	v_fma_mix_f32 v30, v18, v53, v11 op_sel:[0,1,0] op_sel_hi:[0,1,0]
	v_fma_mix_f32 v19, v18, v52, v11 op_sel_hi:[0,1,0]
	v_fma_mix_f32 v23, v18, v53, v11 op_sel_hi:[0,1,0]
	v_fma_mix_f32 v34, v18, v54, v11 op_sel_hi:[0,1,0]
	v_fma_mix_f32 v35, v18, v54, v11 op_sel:[0,1,0] op_sel_hi:[0,1,0]
	v_fma_mix_f32 v38, v18, v55, v11 op_sel_hi:[0,1,0]
	v_fma_mix_f32 v18, v18, v55, v11 op_sel:[0,1,0] op_sel_hi:[0,1,0]
	s_waitcnt vmcnt(4)
	v_fma_mix_f32 v22, v10, v48, v22 op_sel:[0,1,0] op_sel_hi:[0,1,0]
	v_fma_mix_f32 v30, v10, v49, v30 op_sel:[0,1,0] op_sel_hi:[0,1,0]
	v_cmp_lt_i32_e32 vcc, -1, v7
	v_fma_mix_f32 v19, v10, v48, v19 op_sel_hi:[0,1,0]
	v_fma_mix_f32 v23, v10, v49, v23 op_sel_hi:[0,1,0]
	v_fma_mix_f32 v39, v10, v50, v34 op_sel_hi:[0,1,0]
	v_fma_mix_f32 v35, v10, v50, v35 op_sel:[0,1,0] op_sel_hi:[0,1,0]
	v_fma_mix_f32 v43, v10, v51, v38 op_sel_hi:[0,1,0]
	v_fma_mix_f32 v48, v10, v51, v18 op_sel:[0,1,0] op_sel_hi:[0,1,0]
	s_waitcnt vmcnt(3)
	v_fma_mix_f32 v42, v6, v44, v19 op_sel_hi:[0,1,0]
	v_fma_mix_f32 v38, v6, v44, v22 op_sel:[0,1,0] op_sel_hi:[0,1,0]
	v_fma_mix_f32 v34, v6, v45, v23 op_sel_hi:[0,1,0]
	v_fma_mix_f32 v30, v6, v45, v30 op_sel:[0,1,0] op_sel_hi:[0,1,0]
	v_fma_mix_f32 v22, v6, v46, v39 op_sel_hi:[0,1,0]
	v_fma_mix_f32 v18, v6, v46, v35 op_sel:[0,1,0] op_sel_hi:[0,1,0]
	v_fma_mix_f32 v10, v6, v47, v43 op_sel_hi:[0,1,0]
	v_fma_mix_f32 v6, v6, v47, v48 op_sel:[0,1,0] op_sel_hi:[0,1,0]
	s_and_saveexec_b64 s[2:3], vcc
	ds_read_b32 v11, v31 offset:548
	s_or_b64 exec, exec, s[2:3]
	s_load_dwordx2 s[0:1], s[0:1], 0x18
	s_ashr_i32 s5, s4, 31
	v_mov_b32_e32 v7, 0
	v_mov_b32_e32 v19, 0
	s_and_saveexec_b64 s[2:3], vcc
	ds_read_b32 v19, v31 offset:552
	s_or_b64 exec, exec, s[2:3]
	s_and_saveexec_b64 s[2:3], vcc
	ds_read_b32 v7, v31 offset:556
	s_or_b64 exec, exec, s[2:3]
	v_mov_b32_e32 v23, 0
	s_waitcnt vmcnt(2) lgkmcnt(0)
	v_fma_mix_f32 v31, v11, v24, v23 op_sel_hi:[0,1,0]
	v_fma_mix_f32 v24, v11, v24, v23 op_sel:[0,1,0] op_sel_hi:[0,1,0]
	v_fma_mix_f32 v35, v11, v25, v23 op_sel_hi:[0,1,0]
	v_fma_mix_f32 v25, v11, v25, v23 op_sel:[0,1,0] op_sel_hi:[0,1,0]
	v_fma_mix_f32 v39, v11, v26, v23 op_sel_hi:[0,1,0]
	v_fma_mix_f32 v26, v11, v26, v23 op_sel:[0,1,0] op_sel_hi:[0,1,0]
	v_fma_mix_f32 v43, v11, v27, v23 op_sel_hi:[0,1,0]
	v_fma_mix_f32 v11, v11, v27, v23 op_sel:[0,1,0] op_sel_hi:[0,1,0]
	s_waitcnt vmcnt(1)
	v_fma_mix_f32 v23, v19, v12, v31 op_sel_hi:[0,1,0]
	s_lshl_b64 s[2:3], s[4:5], 24
	v_fma_mix_f32 v12, v19, v12, v24 op_sel:[0,1,0] op_sel_hi:[0,1,0]
	v_fma_mix_f32 v24, v19, v13, v35 op_sel_hi:[0,1,0]
	v_fma_mix_f32 v13, v19, v13, v25 op_sel:[0,1,0] op_sel_hi:[0,1,0]
	v_fma_mix_f32 v25, v19, v14, v39 op_sel_hi:[0,1,0]
	v_fma_mix_f32 v14, v19, v14, v26 op_sel:[0,1,0] op_sel_hi:[0,1,0]
	v_fma_mix_f32 v26, v19, v15, v43 op_sel_hi:[0,1,0]
	v_fma_mix_f32 v15, v19, v15, v11 op_sel:[0,1,0] op_sel_hi:[0,1,0]
	s_add_u32 s0, s0, s2
	s_addc_u32 s1, s1, s3
	s_add_u32 s2, s0, 0x100000
	s_addc_u32 s3, s1, 0
	s_add_u32 s4, s0, 0x200000
	s_addc_u32 s5, s1, 0
	s_add_u32 s6, s0, 0x300000
	s_addc_u32 s7, s1, 0
	s_add_u32 s8, s0, 0x400000
	s_addc_u32 s9, s1, 0
	s_add_u32 s10, s0, 0x500000
	s_addc_u32 s11, s1, 0
	s_add_u32 s12, s0, 0x600000
	s_addc_u32 s13, s1, 0
	s_add_u32 s14, s0, 0x700000
	s_addc_u32 s15, s1, 0
	s_waitcnt vmcnt(0)
	v_fma_mix_f32 v43, v7, v0, v23 op_sel_hi:[0,1,0]
	v_fma_mix_f32 v23, v7, v2, v25 op_sel_hi:[0,1,0]
	v_fma_mix_f32 v19, v7, v2, v14 op_sel:[0,1,0] op_sel_hi:[0,1,0]
	v_fma_mix_f32 v39, v7, v0, v12 op_sel:[0,1,0] op_sel_hi:[0,1,0]
	v_fma_mix_f32 v35, v7, v1, v24 op_sel_hi:[0,1,0]
	v_fma_mix_f32 v31, v7, v1, v13 op_sel:[0,1,0] op_sel_hi:[0,1,0]
	v_fma_mix_f32 v11, v7, v3, v26 op_sel_hi:[0,1,0]
	v_fma_mix_f32 v7, v7, v3, v15 op_sel:[0,1,0] op_sel_hi:[0,1,0]
	ds_write_b128 v68, v[40:43]
	ds_write_b128 v68, v[36:39] offset:512
	ds_write_b128 v68, v[32:35] offset:1024
	ds_write_b128 v68, v[28:31] offset:1536
	ds_read_b128 v[44:47], v71
	ds_read_b128 v[48:51], v71 offset:512
	ds_read_b128 v[52:55], v71 offset:1024
	ds_read_b128 v[56:59], v71 offset:1536
	ds_write_b128 v68, v[20:23]
	ds_write_b128 v68, v[16:19] offset:512
	ds_write_b128 v68, v[8:11] offset:1024
	ds_write_b128 v68, v[4:7] offset:1536
	s_waitcnt lgkmcnt(7)
	global_store_dwordx4 v70, v[44:47], s[0:1] nt
	s_waitcnt lgkmcnt(6)
	global_store_dwordx4 v70, v[48:51], s[2:3] nt
	s_waitcnt lgkmcnt(5)
	global_store_dwordx4 v70, v[52:55], s[4:5] nt
	s_waitcnt lgkmcnt(4)
	global_store_dwordx4 v70, v[56:59], s[6:7] nt
	ds_read_b128 v[60:63], v71
	ds_read_b128 v[64:67], v71 offset:512
	ds_read_b128 v[0:3], v71 offset:1024
	ds_read_b128 v[12:15], v71 offset:1536
	s_waitcnt lgkmcnt(3)
	global_store_dwordx4 v70, v[60:63], s[8:9] nt
	s_waitcnt lgkmcnt(2)
	global_store_dwordx4 v70, v[64:67], s[10:11] nt
	s_waitcnt lgkmcnt(1)
	global_store_dwordx4 v70, v[0:3], s[12:13] nt
	s_waitcnt lgkmcnt(0)
	global_store_dwordx4 v70, v[12:15], s[14:15] nt
	s_endpgm

	.amdhsa_kernel _Z6interpPKiPKfPK15HIP_vector_typeIjLj4EEPf
		.amdhsa_group_segment_fixed_size 16384
		.amdhsa_private_segment_fixed_size 0
		.amdhsa_kernarg_size 32
		.amdhsa_user_sgpr_count 2
		.amdhsa_user_sgpr_dispatch_ptr 0
		.amdhsa_user_sgpr_queue_ptr 0
		.amdhsa_user_sgpr_kernarg_segment_ptr 1
		.amdhsa_user_sgpr_dispatch_id 0
		.amdhsa_user_sgpr_kernarg_preload_length 0
		.amdhsa_user_sgpr_kernarg_preload_offset 0
		.amdhsa_user_sgpr_private_segment_size 0
		.amdhsa_uses_dynamic_stack 0
		.amdhsa_enable_private_segment 0
		.amdhsa_system_sgpr_workgroup_id_x 1
		.amdhsa_system_sgpr_workgroup_id_y 0
		.amdhsa_system_sgpr_workgroup_id_z 0
		.amdhsa_system_sgpr_workgroup_info 0
		.amdhsa_system_vgpr_workitem_id 0
		.amdhsa_next_free_vgpr 72
		.amdhsa_next_free_sgpr 16
		.amdhsa_accum_offset 72
		.amdhsa_reserve_vcc 1
		.amdhsa_float_round_mode_32 0
		.amdhsa_float_round_mode_16_64 0
		.amdhsa_float_denorm_mode_32 3
		.amdhsa_float_denorm_mode_16_64 3
		.amdhsa_dx10_clamp 1
		.amdhsa_ieee_mode 1
		.amdhsa_fp16_overflow 0
		.amdhsa_tg_split 0
		.amdhsa_exception_fp_ieee_invalid_op 0
		.amdhsa_exception_fp_denorm_src 0
		.amdhsa_exception_fp_ieee_div_zero 0
		.amdhsa_exception_fp_ieee_overflow 0
		.amdhsa_exception_fp_ieee_underflow 0
		.amdhsa_exception_fp_ieee_inexact 0
		.amdhsa_exception_int_div_zero 0
	.end_amdhsa_kernel

amdhsa.kernels:
  - .agpr_count:     0
    .args:
      - .actual_access:  read_only
        .address_space:  global
        .offset:         0
        .size:           8
        .value_kind:     global_buffer
      - .actual_access:  write_only
        .address_space:  global
        .offset:         8
        .size:           8
        .value_kind:     global_buffer
      - .address_space:  global
        .offset:         16
        .size:           8
        .value_kind:     global_buffer
      - .address_space:  global
        .offset:         24
        .size:           8
        .value_kind:     global_buffer
    .group_segment_fixed_size: 0
    .kernarg_segment_align: 8
    .kernarg_segment_size: 32
    .language:       OpenCL C
    .language_version:
      - 2
      - 0
    .max_flat_workgroup_size: 256
    .name:           _Z13convert_tablePKfP15HIP_vector_typeIjLj4EEPKiS0_
    .private_segment_fixed_size: 0
    .sgpr_count:     18
    .sgpr_spill_count: 0
    .symbol:         _Z13convert_tablePKfP15HIP_vector_typeIjLj4EEPKiS0_.kd
    .uniform_work_group_size: 1
    .uses_dynamic_stack: false
    .vgpr_count:     16
    .vgpr_spill_count: 0
    .wavefront_size: 64
  - .agpr_count:     0
    .args:
      - .address_space:  global
        .offset:         0
        .size:           8
        .value_kind:     global_buffer
      - .address_space:  global
        .offset:         8
        .size:           8
        .value_kind:     global_buffer
      - .actual_access:  read_only
        .address_space:  global
        .offset:         16
        .size:           8
        .value_kind:     global_buffer
      - .address_space:  global
        .offset:         24
        .size:           8
        .value_kind:     global_buffer
    .group_segment_fixed_size: 16384
    .kernarg_segment_align: 8
    .kernarg_segment_size: 32
    .language:       OpenCL C
    .language_version:
      - 2
      - 0
    .max_flat_workgroup_size: 256
    .name:           _Z6interpPKiPKfPK15HIP_vector_typeIjLj4EEPf
    .private_segment_fixed_size: 0
    .sgpr_count:     22
    .sgpr_spill_count: 0
    .symbol:         _Z6interpPKiPKfPK15HIP_vector_typeIjLj4EEPf.kd
    .uniform_work_group_size: 1
    .uses_dynamic_stack: false
    .vgpr_count:     72
    .vgpr_spill_count: 0
    .wavefront_size: 64
